# passCU: block-index priority raise (second resident block) instead of the upper-half-waves raise
# speedup vs baseline: 1.0042x; 1.0042x over previous
.LBB8_4:
	s_load_dwordx2 s[12:13], s[0:1], 0xa8
	s_load_dwordx2 s[18:19], s[0:1], 0x98
	s_waitcnt lgkmcnt(0)
	s_sub_i32 s4, s28, s20
	s_add_i32 s4, s4, 31
	v_and_b32_e32 v1, 63, v0
	s_ashr_i32 s15, s4, 5
	s_cmp_lt_i32 s15, 1
	v_add_u32_e32 v90, s14, v98
	v_and_b32_e32 v100, 32, v0
	v_lshlrev_b32_e32 v99, 4, v1
	s_cbranch_scc1 .LBB8_7
	s_load_dwordx8 s[4:11], s[0:1], 0x0
	s_load_dwordx2 s[24:25], s[0:1], 0x20
	s_load_dwordx2 s[30:31], s[0:1], 0x80
	s_load_dwordx2 s[48:49], s[0:1], 0x90
	v_and_b32_e32 v34, 7, v1
	v_lshlrev_b32_e32 v34, 4, v34
	v_lshrrev_b32_e32 v35, 3, v1
	s_lshl_b32 s32, s3, 12
	s_add_i32 s33, s32, 0x2000
	s_add_i32 s32, s32, 0xb500
	s_cmp_lt_u32 s3, 2
	s_cselect_b32 s32, s33, s32
	v_lshlrev_b32_e32 v36, 1, v35
	v_and_b32_e32 v36, 7, v36
	v_or_b32_e32 v37, 1, v36
	v_lshlrev_b32_e32 v36, 4, v36
	v_lshlrev_b32_e32 v37, 4, v37
	v_xor_b32_e32 v36, v36, v34
	v_xor_b32_e32 v37, v37, v34
	v_lshl_add_u32 v39, v35, 9, s32
	v_add_u32_e32 v36, v36, v39
	v_add_u32_e32 v37, v37, v39
	v_lshrrev_b32_e32 v38, 1, v98
	v_and_b32_e32 v38, 7, v38
	v_lshrrev_b32_e32 v39, 3, v100
	v_xor_b32_e32 v38, v38, v39
	v_lshlrev_b32_e32 v38, 4, v38
	v_lshl_add_u32 v39, v98, 7, s32
	v_add_u32_e32 v38, v38, v39
	v_lshlrev_b32_e32 v35, 4, v35
	s_mov_b32 s35, 0x1869f
	s_mov_b32 s65, 0xffff0000
	v_mov_b32_e32 v2, 0
	v_mov_b32_e32 v3, 0
	v_mov_b32_e32 v4, 0
	v_mov_b32_e32 v5, 0
	v_mov_b32_e32 v6, 0
	v_mov_b32_e32 v7, 0
	v_mov_b32_e32 v8, 0
	v_mov_b32_e32 v9, 0
	v_mov_b32_e32 v10, 0
	v_mov_b32_e32 v11, 0
	v_mov_b32_e32 v12, 0
	v_mov_b32_e32 v13, 0
	v_mov_b32_e32 v14, 0
	v_mov_b32_e32 v15, 0
	v_mov_b32_e32 v16, 0
	v_mov_b32_e32 v17, 0
	v_mov_b32_e32 v18, 0
	v_mov_b32_e32 v19, 0
	v_mov_b32_e32 v20, 0
	v_mov_b32_e32 v21, 0
	v_mov_b32_e32 v22, 0
	v_mov_b32_e32 v23, 0
	v_mov_b32_e32 v24, 0
	v_mov_b32_e32 v25, 0
	v_mov_b32_e32 v26, 0
	v_mov_b32_e32 v27, 0
	v_mov_b32_e32 v28, 0
	v_mov_b32_e32 v29, 0
	v_mov_b32_e32 v30, 0
	v_mov_b32_e32 v31, 0
	v_mov_b32_e32 v32, 0
	v_mov_b32_e32 v33, 0
	s_waitcnt vmcnt(0) lgkmcnt(0)
	v_mov_b32_e32 v42, v70
	v_mov_b32_e32 v43, v71
	v_mov_b32_e32 v44, v72
	v_mov_b32_e32 v45, v73
	v_mov_b32_e32 v46, v74
	v_mov_b32_e32 v47, v75
	v_mov_b32_e32 v48, v76
	v_mov_b32_e32 v49, v77
	v_mov_b32_e32 v50, v78
	v_mov_b32_e32 v51, v79
	v_mov_b32_e32 v52, v80
	v_mov_b32_e32 v53, v81
	v_lshlrev_b32_e32 v39, 2, v90
	global_load_dword v40, v39, s[30:31]
	global_load_dword v41, v39, s[30:31] offset:4
	s_lshl_b32 s34, s20, 2
	v_min_u32_e32 v42, s35, v42
	v_min_u32_e32 v46, s35, v46
	v_min_u32_e32 v43, s35, v43
	v_min_u32_e32 v47, s35, v47
	v_min_u32_e32 v44, s35, v44
	v_min_u32_e32 v48, s35, v48
	v_min_u32_e32 v45, s35, v45
	v_min_u32_e32 v49, s35, v49
	v_lshl_or_b32 v42, v42, 7, v34
	v_lshl_or_b32 v46, v46, 7, v34
	v_lshl_or_b32 v43, v43, 7, v34
	v_lshl_or_b32 v47, v47, 7, v34
	v_lshl_or_b32 v44, v44, 7, v34
	v_lshl_or_b32 v48, v48, 7, v34
	v_lshl_or_b32 v45, v45, 7, v34
	v_lshl_or_b32 v49, v49, 7, v34
	global_load_dwordx4 v[70:73], v42, s[24:25]
	global_load_dwordx4 v[74:77], v43, s[24:25]
	global_load_dwordx4 v[78:81], v44, s[24:25]
	global_load_dwordx4 v[82:85], v45, s[24:25]
	global_load_dwordx4 v[86:89], v46, s[10:11]
	global_load_dwordx4 v[90:93], v47, s[10:11]
	global_load_dwordx4 v[94:97], v48, s[10:11]
	global_load_dwordx4 v[102:105], v49, s[10:11]
	s_add_i32 s34, s34, 0x80
	v_add_u32_e32 v39, s34, v35
	global_load_dwordx4 v[42:45], v39, s[4:5]
	global_load_dwordx4 v[46:49], v39, s[6:7]
	s_bitcmp1_b32 s2, 8
	s_cbranch_scc0 .Lcu_nopri
	s_setprio 1
